# SSD scan: per-chunk decay prefix/suffix sums via DPP row shifts + row-total adds instead of six dependent ds_bpermute hops
# baseline (speedup 1.0000x reference)
; __device__ __forceinline__ float shl_from(float v, int src_lane) { return __int_as_float(__builtin_amdgcn_ds_bpermute(src_lane << 2, __float_as_int(v))); }
; __device__ __forceinline__ void ssd_unit(const Frame& F, int layer, int unit) {
;     ...
;         if (wave == 7) {
;             const float d0 = rd0, d1 = rd1;
;             const float da0 = d0 * a_coef, da1 = d1 * a_coef; const float ps = da0 + da1;
;             float inc = ps; float c0v, c1v;
;             if (dir == 0) {
; #pragma unroll
;                 for (int o = 1; o < 64; o <<= 1) { const float t = shl_from(inc, lane2 - o); if (lane2 >= o) inc += t; }
;                 c0v = inc - da1; c1v = inc;
;             } else {
; #pragma unroll
;                 for (int o = 1; o < 64; o <<= 1) { const float t = shl_from(inc, lane2 + o); if (lane2 + o < 64) inc += t; }
;                 c0v = inc; c1v = inc - da0;
;             }
;             const float tot = shl_from(inc, dir ? 0 : 63);
.LBB0_665:
	v_cndmask_b32_e64 v16, 0, 1, s[74:75]
	v_mov_b32_e32 v24, v133
	v_mov_b32_e32 v20, v252
	v_cmp_ne_u32_e64 s[44:45], 1, v16
	s_andn2_b64 vcc, exec, s[74:75]
	s_cbranch_vccnz .LBB0_673
	s_waitcnt vmcnt(16)
	v_mul_f32_e64 v21, v123, -v144
	v_fma_f32 v23, v122, -v144, v21
	v_lshlrev_b32_e32 v22, 2, v20
	s_mov_b64 s[2:3], -1
	s_and_b64 vcc, exec, s[42:43]
	v_cmp_gt_i32_e64 s[46:47], 32, v20
	s_cbranch_vccnz .LBB0_668
	v_mul_f32_e64 v19, v122, -v144
	s_mov_b64 s[2:3], 0
	v_mov_b32_e32 v18, v23
	s_nop 1
	v_add_f32_dpp v18, v18, v18 row_shl:1 row_mask:0xf bank_mask:0xf bound_ctrl:1
	s_nop 1
	v_add_f32_dpp v18, v18, v18 row_shl:2 row_mask:0xf bank_mask:0xf bound_ctrl:1
	s_nop 1
	v_add_f32_dpp v18, v18, v18 row_shl:4 row_mask:0xf bank_mask:0xf bound_ctrl:1
	s_nop 1
	v_add_f32_dpp v18, v18, v18 row_shl:8 row_mask:0xf bank_mask:0xf bound_ctrl:1
	s_nop 1
	v_readlane_b32 s46, v18, 48
	v_readlane_b32 s47, v18, 32
	v_readlane_b32 vcc_lo, v18, 16
	s_mov_b32 exec_hi, 0xffff
	s_nop 1
	v_add_f32_e32 v18, s46, v18
	s_mov_b32 exec_hi, 0
	v_add_f32_e32 v18, s47, v18
	s_mov_b32 exec_lo, 0xffff
	v_add_f32_e32 v18, vcc_lo, v18
	s_mov_b64 exec, -1
	v_sub_f32_e32 v19, v18, v19
	v_mov_b64_e32 v[16:17], v[18:19]
.LBB0_668:
	s_mov_b32 s4, 0
	s_andn2_b64 vcc, exec, s[2:3]
	v_mov_b32_e32 v25, v18
	s_cbranch_vccnz .LBB0_670
	s_movk_i32 s4, 0xfc
	v_mov_b32_e32 v17, v23
	s_nop 1
	v_add_f32_dpp v17, v17, v17 row_shr:1 row_mask:0xf bank_mask:0xf bound_ctrl:1
	s_nop 1
	v_add_f32_dpp v17, v17, v17 row_shr:2 row_mask:0xf bank_mask:0xf bound_ctrl:1
	s_nop 1
	v_add_f32_dpp v17, v17, v17 row_shr:4 row_mask:0xf bank_mask:0xf bound_ctrl:1
	s_nop 1
	v_add_f32_dpp v17, v17, v17 row_shr:8 row_mask:0xf bank_mask:0xf bound_ctrl:1
	s_nop 1
	v_readlane_b32 s46, v17, 15
	v_readlane_b32 s47, v17, 31
	v_readlane_b32 vcc_lo, v17, 47
	s_mov_b32 exec_lo, 0xffff0000
	s_nop 1
	v_add_f32_e32 v17, s46, v17
	s_mov_b32 exec_lo, 0
	v_add_f32_e32 v17, s47, v17
	s_mov_b32 exec_hi, 0xffff0000
	v_add_f32_e32 v17, vcc_lo, v17
	s_mov_b64 exec, -1
	v_sub_f32_e32 v16, v17, v21
	v_mov_b32_e32 v18, v17
	v_mov_b32_e32 v25, v16
	v_mov_b32_e32 v19, v17
